# router phase: second W1-conversion slice rides in the last four 16-token groups (experts 14,15; those groups have less x traffic), stand-alone conversion stops at expert 13 on the 256-WG grid
# baseline (speedup 1.0000x reference)
.LBB0_729:
	s_ashr_i32 s26, s52, 12
	s_add_i32 s46, s26, 28
	s_ashr_i32 s47, s46, 31
	s_lshl_b64 s[26:27], s[46:47], 25
	s_add_u32 s26, s30, s26
	s_addc_u32 s27, s31, s27
	s_lshr_b32 s40, s52, 1
	s_and_b32 s40, s40, 0x7c0
	v_add_lshl_u32 v32, s40, v76, 12
	s_and_b32 s48, s53, 0xfe0
	v_or3_b32 v82, v32, v160, s48
	v_lshl_add_u64 v[56:57], v[82:83], 2, s[26:27]
	s_cmpk_lg_i32 s99, 0x100
	s_cbranch_scc1 .Lp5dbl_noissue
	s_cmp_lt_u32 s77, 4
	s_cbranch_scc1 .Lp5dbl_noissue
	s_sub_u32 vcc_lo, s26, 0x20000000
	s_subb_u32 vcc_hi, s27, 0
	v_lshlrev_b32_e32 v226, 2, v82
	v_add_u32_e32 v230, s64, v226
	v_add_u32_e32 v234, s65, v226
	v_add_u32_e32 v238, s66, v226
	v_add_u32_e32 v242, s67, v226
	v_add_u32_e32 v246, s68, v226
	v_add_u32_e32 v250, s69, v226
	v_add_u32_e32 v178, s70, v226
	global_load_dwordx4 v[226:229], v226, vcc nt
	global_load_dwordx4 v[230:233], v230, vcc nt
	global_load_dwordx4 v[234:237], v234, vcc nt
	global_load_dwordx4 v[238:241], v238, vcc nt
	global_load_dwordx4 v[242:245], v242, vcc nt
	global_load_dwordx4 v[246:249], v246, vcc nt
	global_load_dwordx4 v[250:253], v250, vcc nt
	global_load_dwordx4 v[178:181], v178, vcc nt

.LBB0_734:
	v_mul_f32_e32 v32, 0x43800000, v32
	v_mul_f32_e32 v36, 0x43800000, v36
	v_mov_b32_e32 v66, v83
	v_cvt_pk_fp8_f32 v66, v32, v36
	v_mul_f32_e32 v32, 0x43800000, v48
	v_mul_f32_e32 v36, 0x43800000, v52
	v_mov_b32_e32 v67, v83
	v_cvt_pk_fp8_f32 v67, v32, v36
	v_mul_f32_e32 v32, 0x43800000, v56
	v_mul_f32_e32 v36, 0x43800000, v60
	s_lshr_b32 s26, s53, 8
	v_cvt_pk_fp8_f32 v67, v32, v36 op_sel:[0,0,1]
	v_mul_f32_e32 v33, 0x43800000, v33
	v_mul_f32_e32 v36, 0x43800000, v37
	v_mov_b32_e32 v32, v83
	s_and_b32 s26, s26, 8
	v_mul_f32_e32 v37, 0x43800000, v41
	v_cvt_pk_fp8_f32 v32, v33, v36
	v_mul_f32_e32 v36, 0x43800000, v49
	v_mul_f32_e32 v41, 0x43800000, v53
	v_mov_b32_e32 v33, v83
	s_or_b32 s48, s50, s26
	s_lshl_b64 s[26:27], s[46:47], 12
	v_cvt_pk_fp8_f32 v33, v36, v41
	s_or_b32 s26, s26, s48
	v_mul_f32_e32 v40, 0x43800000, v40
	v_mul_f32_e32 v44, 0x43800000, v44
	s_waitcnt lgkmcnt(0)
	v_mov_b32_e32 v65, s27
	v_or_b32_e32 v64, s26, v80
	v_cvt_pk_fp8_f32 v66, v40, v44 op_sel:[0,0,1]
	v_mul_f32_e32 v40, 0x43800000, v45
	v_lshlrev_b64 v[64:65], 11, v[64:65]
	v_cvt_pk_fp8_f32 v32, v37, v40 op_sel:[0,0,1]
	v_mul_f32_e32 v36, 0x43800000, v57
	v_mul_f32_e32 v37, 0x43800000, v61
	v_lshl_add_u64 v[64:65], s[28:29], 0, v[64:65]
	v_cvt_pk_fp8_f32 v33, v36, v37 op_sel:[0,0,1]
	v_lshl_add_u64 v[36:37], v[64:65], 0, s[40:41]
	v_lshl_add_u64 v[36:37], v[36:37], 0, v[76:77]
	global_store_dwordx2 v[36:37], v[66:67], off
	global_store_dwordx2 v[36:37], v[32:33], off offset:2048
	v_mul_f32_e32 v33, 0x43800000, v34
	v_mul_f32_e32 v34, 0x43800000, v38
	v_mov_b32_e32 v32, v83
	v_cvt_pk_fp8_f32 v32, v33, v34
	v_mul_f32_e32 v34, 0x43800000, v50
	v_mul_f32_e32 v41, 0x43800000, v54
	v_mov_b32_e32 v33, v83
	v_cvt_pk_fp8_f32 v33, v34, v41
	v_mul_f32_e32 v38, 0x43800000, v42
	v_mul_f32_e32 v40, 0x43800000, v46
	v_cvt_pk_fp8_f32 v32, v38, v40 op_sel:[0,0,1]
	v_mul_f32_e32 v34, 0x43800000, v58
	v_mul_f32_e32 v38, 0x43800000, v62
	v_cvt_pk_fp8_f32 v33, v34, v38 op_sel:[0,0,1]
	v_mul_f32_e32 v35, 0x43800000, v35
	v_mul_f32_e32 v38, 0x43800000, v39
	v_mov_b32_e32 v34, v83
	v_cvt_pk_fp8_f32 v34, v35, v38
	v_mul_f32_e32 v38, 0x43800000, v51
	v_mul_f32_e32 v41, 0x43800000, v55
	v_mov_b32_e32 v35, v83
	v_cvt_pk_fp8_f32 v35, v38, v41
	v_mul_f32_e32 v39, 0x43800000, v43
	v_mul_f32_e32 v40, 0x43800000, v47
	v_cvt_pk_fp8_f32 v34, v39, v40 op_sel:[0,0,1]
	v_mul_f32_e32 v38, 0x43800000, v59
	v_mul_f32_e32 v39, 0x43800000, v63
	v_cvt_pk_fp8_f32 v35, v38, v39 op_sel:[0,0,1]
	v_add_co_u32_e32 v36, vcc, s72, v36
	v_add_u32_e32 v38, s49, v164
	s_nop 0
	v_addc_co_u32_e32 v37, vcc, 0, v37, vcc
	global_store_dwordx2 v[36:37], v[32:33], off
	global_store_dwordx2 v[36:37], v[34:35], off offset:2048
	s_cmpk_lg_i32 s99, 0x100
	s_cbranch_scc1 .Lp5dbl_noconsume
	s_cmp_lt_u32 s77, 4
	s_cbranch_scc1 .Lp5dbl_noconsume
	s_sub_i32 s46, s46, 16
	v_mul_f32_e32 v226, 0x43800000, v226
	v_mul_f32_e32 v230, 0x43800000, v230
	v_mov_b32_e32 v66, v83
	v_cvt_pk_fp8_f32 v66, v226, v230
	v_mul_f32_e32 v226, 0x43800000, v242
	v_mul_f32_e32 v230, 0x43800000, v246
	v_mov_b32_e32 v67, v83
	v_cvt_pk_fp8_f32 v67, v226, v230
	v_mul_f32_e32 v226, 0x43800000, v250
	v_mul_f32_e32 v230, 0x43800000, v178
	s_lshr_b32 s26, s53, 8
	v_cvt_pk_fp8_f32 v67, v226, v230 op_sel:[0,0,1]
	v_mul_f32_e32 v227, 0x43800000, v227
	v_mul_f32_e32 v230, 0x43800000, v231
	v_mov_b32_e32 v226, v83
	s_and_b32 s26, s26, 8
	v_mul_f32_e32 v231, 0x43800000, v235
	v_cvt_pk_fp8_f32 v226, v227, v230
	v_mul_f32_e32 v230, 0x43800000, v243
	v_mul_f32_e32 v235, 0x43800000, v247
	v_mov_b32_e32 v227, v83
	s_or_b32 s48, s50, s26
	s_lshl_b64 s[26:27], s[46:47], 12
	v_cvt_pk_fp8_f32 v227, v230, v235
	s_or_b32 s26, s26, s48
	v_mul_f32_e32 v234, 0x43800000, v234
	v_mul_f32_e32 v238, 0x43800000, v238
	s_waitcnt lgkmcnt(0)
	v_mov_b32_e32 v65, s27
	v_or_b32_e32 v64, s26, v80
	v_cvt_pk_fp8_f32 v66, v234, v238 op_sel:[0,0,1]
	v_mul_f32_e32 v234, 0x43800000, v239
	v_lshlrev_b64 v[64:65], 11, v[64:65]
	v_cvt_pk_fp8_f32 v226, v231, v234 op_sel:[0,0,1]
	v_mul_f32_e32 v230, 0x43800000, v251
	v_mul_f32_e32 v231, 0x43800000, v179
	v_lshl_add_u64 v[64:65], s[28:29], 0, v[64:65]
	v_cvt_pk_fp8_f32 v227, v230, v231 op_sel:[0,0,1]
	v_lshl_add_u64 v[230:231], v[64:65], 0, s[40:41]
	v_lshl_add_u64 v[230:231], v[230:231], 0, v[76:77]
	global_store_dwordx2 v[230:231], v[66:67], off
	global_store_dwordx2 v[230:231], v[226:227], off offset:2048
	v_mul_f32_e32 v227, 0x43800000, v228
	v_mul_f32_e32 v228, 0x43800000, v232
	v_mov_b32_e32 v226, v83
	v_cvt_pk_fp8_f32 v226, v227, v228
	v_mul_f32_e32 v228, 0x43800000, v244
	v_mul_f32_e32 v235, 0x43800000, v248
	v_mov_b32_e32 v227, v83
	v_cvt_pk_fp8_f32 v227, v228, v235
	v_mul_f32_e32 v232, 0x43800000, v236
	v_mul_f32_e32 v234, 0x43800000, v240
	v_cvt_pk_fp8_f32 v226, v232, v234 op_sel:[0,0,1]
	v_mul_f32_e32 v228, 0x43800000, v252
	v_mul_f32_e32 v232, 0x43800000, v180
	v_cvt_pk_fp8_f32 v227, v228, v232 op_sel:[0,0,1]
	v_mul_f32_e32 v229, 0x43800000, v229
	v_mul_f32_e32 v232, 0x43800000, v233
	v_mov_b32_e32 v228, v83
	v_cvt_pk_fp8_f32 v228, v229, v232
	v_mul_f32_e32 v232, 0x43800000, v245
	v_mul_f32_e32 v235, 0x43800000, v249
	v_mov_b32_e32 v229, v83
	v_cvt_pk_fp8_f32 v229, v232, v235
	v_mul_f32_e32 v233, 0x43800000, v237
	v_mul_f32_e32 v234, 0x43800000, v241
	v_cvt_pk_fp8_f32 v228, v233, v234 op_sel:[0,0,1]
	v_mul_f32_e32 v232, 0x43800000, v253
	v_mul_f32_e32 v233, 0x43800000, v181
	v_cvt_pk_fp8_f32 v229, v232, v233 op_sel:[0,0,1]
	v_add_co_u32_e32 v230, vcc, s72, v230
	v_add_u32_e32 v232, s49, v164
	s_nop 0
	v_addc_co_u32_e32 v231, vcc, 0, v231, vcc
	global_store_dwordx2 v[230:231], v[226:227], off
	global_store_dwordx2 v[230:231], v[228:229], off offset:2048
